# P7 merge epilogue VALU runs list-scheduled (renamed v2 temps, dependent ops spread apart)
# baseline (speedup 1.0000x reference)
.LBB0_1047:
	s_lshl_b32 s4, s64, 8
	v_mov_b32_e32 v148, v0
	s_add_i32 s4, s4, s58
	s_mov_b32 s12, 0x20000
	v_and_or_b32 v212, v148, 15, s4
	s_lshl_b32 s4, s63, 6
	s_or_b32 s4, s4, s61
	v_lshrrev_b32_e32 v2, 2, v148
	v_and_or_b32 v214, v2, 12, s4
	v_ashrrev_i32_e32 v213, 31, v212
	v_ashrrev_i32_e32 v140, 3, v214
	v_lshlrev_b64 v[144:145], 3, v[212:213]
	v_ashrrev_i32_e32 v141, 31, v140
	v_and_b32_e32 v147, 0x3fffff, v145
	v_and_b32_e32 v146, 0xfffffe00, v144
	v_lshl_add_u64 v[146:147], v[146:147], 0, v[140:141]
	v_lshlrev_b64 v[146:147], 10, v[146:147]
	v_lshlrev_b32_e32 v2, 1, v144
	v_lshl_add_u64 v[146:147], s[18:19], 0, v[146:147]
	v_and_b32_e32 v2, 0xf0, v2
	v_lshl_add_u64 v[144:145], v[146:147], 0, v[2:3]
	v_lshrrev_b32_e32 v2, 1, v148
	v_or_b32_e32 v194, 16, v212
	v_and_b32_e32 v2, 8, v2
	v_ashrrev_i32_e32 v195, 31, v194
	v_lshl_add_u64 v[144:145], v[144:145], 0, v[2:3]
	v_lshlrev_b64 v[154:155], 3, v[194:195]
	v_add_co_u32_e32 v146, vcc, s12, v144
	v_and_b32_e32 v157, 0x3fffff, v155
	v_and_b32_e32 v156, 0xfffffe00, v154
	v_addc_co_u32_e32 v147, vcc, 0, v145, vcc
	s_mov_b32 s5, 0x40000
	v_lshl_add_u64 v[156:157], v[156:157], 0, v[140:141]
	v_add_co_u32_e32 v148, vcc, s5, v144
	v_lshlrev_b64 v[156:157], 10, v[156:157]
	v_lshlrev_b32_e32 v154, 1, v154
	v_addc_co_u32_e32 v149, vcc, 0, v145, vcc
	s_mov_b32 s4, 0x60000
	v_lshl_add_u64 v[156:157], s[18:19], 0, v[156:157]
	v_and_b32_e32 v154, 0x3f0, v154
	v_mov_b32_e32 v155, v3
	v_add_co_u32_e32 v150, vcc, s4, v144
	v_lshl_add_u64 v[154:155], v[156:157], 0, v[154:155]
	s_nop 0
	v_addc_co_u32_e32 v151, vcc, 0, v145, vcc
	v_lshl_add_u64 v[154:155], v[154:155], 0, v[2:3]
	v_lshl_add_u64 v[152:153], v[194:195], 2, s[20:21]
	global_load_dwordx2 v[218:219], v[148:149], off
	global_load_dwordx2 v[216:217], v[150:151], off
	global_load_dword v231, v[152:153], off
	global_load_dwordx2 v[204:205], v[154:155], off
	v_add_co_u32_e32 v148, vcc, s12, v154
	v_or_b32_e32 v184, 32, v212
	s_nop 0
	v_addc_co_u32_e32 v149, vcc, 0, v155, vcc
	v_add_co_u32_e32 v150, vcc, s5, v154
	v_ashrrev_i32_e32 v185, 31, v184
	s_nop 0
	v_addc_co_u32_e32 v151, vcc, 0, v155, vcc
	v_add_co_u32_e32 v152, vcc, s4, v154
	v_or_b32_e32 v174, 48, v212
	s_nop 0
	v_addc_co_u32_e32 v153, vcc, 0, v155, vcc
	v_lshl_add_u64 v[154:155], v[184:185], 2, s[20:21]
	global_load_dwordx2 v[210:211], v[148:149], off
	global_load_dwordx2 v[208:209], v[150:151], off
	global_load_dwordx2 v[206:207], v[152:153], off
	global_load_dword v230, v[154:155], off
	v_lshlrev_b64 v[148:149], 3, v[184:185]
	v_and_b32_e32 v151, 0x3fffff, v149
	v_and_b32_e32 v150, 0xfffffe00, v148
	v_lshlrev_b32_e32 v148, 1, v148
	v_mov_b32_e32 v149, v3
	v_lshl_add_u64 v[150:151], v[150:151], 0, v[140:141]
	v_and_b32_e32 v148, 0x3f0, v148
	v_lshlrev_b64 v[150:151], 10, v[150:151]
	v_lshl_add_u64 v[150:151], s[18:19], 0, v[150:151]
	v_lshl_add_u64 v[148:149], v[150:151], 0, v[148:149]
	v_lshl_add_u64 v[148:149], v[148:149], 0, v[2:3]
	v_add_co_u32_e32 v150, vcc, s12, v148
	v_ashrrev_i32_e32 v175, 31, v174
	s_nop 0
	v_addc_co_u32_e32 v151, vcc, 0, v149, vcc
	v_add_co_u32_e32 v152, vcc, s5, v148
	v_lshl_add_u64 v[142:143], v[212:213], 2, s[20:21]
	s_nop 0
	v_addc_co_u32_e32 v153, vcc, 0, v149, vcc
	v_add_co_u32_e32 v154, vcc, s4, v148
	v_add_u32_e32 v164, 0x80, v212
	s_nop 0
	v_addc_co_u32_e32 v155, vcc, 0, v149, vcc
	global_load_dwordx2 v[192:193], v[148:149], off
	global_load_dwordx2 v[190:191], v[150:151], off
	global_load_dwordx2 v[188:189], v[152:153], off
	global_load_dwordx2 v[186:187], v[154:155], off
	v_lshlrev_b64 v[150:151], 3, v[174:175]
	v_and_b32_e32 v153, 0x3fffff, v151
	v_and_b32_e32 v152, 0xfffffe00, v150
	v_lshlrev_b32_e32 v150, 1, v150
	v_mov_b32_e32 v151, v3
	v_lshl_add_u64 v[152:153], v[152:153], 0, v[140:141]
	v_and_b32_e32 v150, 0x3f0, v150
	v_lshlrev_b64 v[152:153], 10, v[152:153]
	v_lshl_add_u64 v[152:153], s[18:19], 0, v[152:153]
	v_lshl_add_u64 v[150:151], v[152:153], 0, v[150:151]
	v_lshl_add_u64 v[150:151], v[150:151], 0, v[2:3]
	v_add_co_u32_e32 v152, vcc, s12, v150
	v_lshl_add_u64 v[148:149], v[174:175], 2, s[20:21]
	s_nop 0
	v_addc_co_u32_e32 v153, vcc, 0, v151, vcc
	v_add_co_u32_e32 v154, vcc, s5, v150
	v_ashrrev_i32_e32 v165, 31, v164
	s_nop 0
	v_addc_co_u32_e32 v155, vcc, 0, v151, vcc
	global_load_dword v229, v[148:149], off
	global_load_dwordx2 v[180:181], v[150:151], off
	global_load_dwordx2 v[178:179], v[152:153], off
	global_load_dwordx2 v[176:177], v[154:155], off
	global_load_dword v232, v[142:143], off
	global_load_dwordx2 v[222:223], v[144:145], off
	global_load_dwordx2 v[220:221], v[146:147], off
	global_load_dword v228, v[142:143], off offset:512
	v_lshlrev_b64 v[142:143], 3, v[164:165]
	v_and_b32_e32 v145, 0x3fffff, v143
	v_and_b32_e32 v144, 0xfffffe00, v142
	v_lshlrev_b32_e32 v142, 1, v142
	v_mov_b32_e32 v143, v3
	v_lshl_add_u64 v[144:145], v[144:145], 0, v[140:141]
	v_and_b32_e32 v142, 0x3f0, v142
	v_lshlrev_b64 v[144:145], 10, v[144:145]
	v_lshl_add_u64 v[144:145], s[18:19], 0, v[144:145]
	v_add_co_u32_e32 v148, vcc, s4, v150
	v_lshl_add_u64 v[142:143], v[144:145], 0, v[142:143]
	s_nop 0
	v_addc_co_u32_e32 v149, vcc, 0, v151, vcc
	v_lshl_add_u64 v[142:143], v[142:143], 0, v[2:3]
	v_add_co_u32_e32 v144, vcc, s12, v142
	v_add_u32_e32 v196, 0xb0, v212
	s_nop 0
	v_addc_co_u32_e32 v145, vcc, 0, v143, vcc
	v_add_co_u32_e32 v146, vcc, s5, v142
	v_ashrrev_i32_e32 v197, 31, v196
	s_nop 0
	v_addc_co_u32_e32 v147, vcc, 0, v143, vcc
	global_load_dwordx2 v[182:183], v[148:149], off
	global_load_dwordx2 v[170:171], v[142:143], off
	global_load_dwordx2 v[168:169], v[144:145], off
	global_load_dwordx2 v[166:167], v[146:147], off
	v_add_u32_e32 v144, 0x90, v212
	v_ashrrev_i32_e32 v145, 31, v144
	v_lshl_add_u64 v[146:147], v[144:145], 2, s[20:21]
	v_lshlrev_b64 v[144:145], 3, v[144:145]
	v_and_b32_e32 v149, 0x3fffff, v145
	v_and_b32_e32 v148, 0xfffffe00, v144
	v_lshlrev_b32_e32 v144, 1, v144
	v_mov_b32_e32 v145, v3
	v_lshl_add_u64 v[148:149], v[148:149], 0, v[140:141]
	v_and_b32_e32 v144, 0x3f0, v144
	v_lshlrev_b64 v[148:149], 10, v[148:149]
	v_lshl_add_u64 v[148:149], s[18:19], 0, v[148:149]
	v_add_co_u32_e32 v142, vcc, s4, v142
	v_lshl_add_u64 v[144:145], v[148:149], 0, v[144:145]
	s_nop 0
	v_addc_co_u32_e32 v143, vcc, 0, v143, vcc
	v_lshl_add_u64 v[144:145], v[144:145], 0, v[2:3]
	v_add_co_u32_e32 v148, vcc, s12, v144
	v_lshl_add_u64 v[198:199], v[196:197], 2, s[20:21]
	s_nop 0
	v_addc_co_u32_e32 v149, vcc, 0, v145, vcc
	global_load_dwordx2 v[172:173], v[142:143], off
	global_load_dword v227, v[146:147], off
	global_load_dwordx2 v[158:159], v[144:145], off
	global_load_dwordx2 v[156:157], v[148:149], off
	v_add_u32_e32 v146, 0xa0, v212
	v_ashrrev_i32_e32 v147, 31, v146
	v_lshl_add_u64 v[148:149], v[146:147], 2, s[20:21]
	v_lshlrev_b64 v[146:147], 3, v[146:147]
	v_and_b32_e32 v151, 0x3fffff, v147
	v_and_b32_e32 v150, 0xfffffe00, v146
	v_lshl_add_u64 v[150:151], v[150:151], 0, v[140:141]
	v_add_co_u32_e32 v142, vcc, s5, v144
	v_lshlrev_b64 v[150:151], 10, v[150:151]
	v_lshlrev_b32_e32 v146, 1, v146
	v_addc_co_u32_e32 v143, vcc, 0, v145, vcc
	v_lshl_add_u64 v[150:151], s[18:19], 0, v[150:151]
	v_and_b32_e32 v146, 0x3f0, v146
	v_mov_b32_e32 v147, v3
	v_add_co_u32_e32 v144, vcc, s4, v144
	v_lshl_add_u64 v[146:147], v[150:151], 0, v[146:147]
	s_nop 0
	v_addc_co_u32_e32 v145, vcc, 0, v145, vcc
	v_lshl_add_u64 v[146:147], v[146:147], 0, v[2:3]
	global_load_dwordx2 v[162:163], v[142:143], off
	global_load_dwordx2 v[160:161], v[144:145], off
	global_load_dword v226, v[148:149], off
	s_nop 0
	global_load_dwordx2 v[148:149], v[146:147], off
	v_add_co_u32_e32 v142, vcc, s12, v146
	s_waitcnt vmcnt(0)
	v_mul_f32_e64 v108, v231, -v108
	v_addc_co_u32_e32 v143, vcc, 0, v147, vcc
	v_add_co_u32_e32 v144, vcc, s5, v146
	v_mul_f32_e64 v124, v232, -v124
	s_nop 0
	v_addc_co_u32_e32 v145, vcc, 0, v147, vcc
	v_add_co_u32_e32 v146, vcc, s4, v146
	v_mul_f32_e32 v124, 0x3fb8aa3b, v124
	s_nop 0
	v_addc_co_u32_e32 v147, vcc, 0, v147, vcc
	global_load_dwordx2 v[154:155], v[142:143], off
	global_load_dwordx2 v[152:153], v[144:145], off
	global_load_dwordx2 v[150:151], v[146:147], off
	global_load_dword v225, v[198:199], off
	v_lshlrev_b64 v[142:143], 3, v[196:197]
	v_mul_f32_e64 v146, v232, -v129
	v_mul_f32_e64 v215, v232, -v130
	v_mul_f32_e64 v235, v232, -v131
	v_mul_f32_e64 v199, v232, -v125
	v_and_b32_e32 v145, 0x3fffff, v143
	v_and_b32_e32 v144, 0xfffffe00, v142
	v_lshlrev_b32_e32 v142, 1, v142
	v_mov_b32_e32 v143, v3
	v_mul_f32_e32 v147, 0x3fb8aa3b, v146
	v_mul_f32_e32 v233, 0x3fb8aa3b, v215
	v_lshl_add_u64 v[140:141], v[144:145], 0, v[140:141]
	v_and_b32_e32 v142, 0x3f0, v142
	v_mul_f32_e32 v236, 0x3fb8aa3b, v235
	v_exp_f32_e32 v198, v147
	v_exp_f32_e32 v234, v233
	v_lshlrev_b64 v[140:141], 10, v[140:141]
	v_exp_f32_e32 v238, v124
	v_exp_f32_e32 v237, v236
	v_mul_f32_e32 v239, 0x3fb8aa3b, v199
	v_mul_f32_e64 v241, v232, -v126
	v_lshl_add_u64 v[140:141], s[18:19], 0, v[140:141]
	v_mul_f32_e64 v244, v232, -v127
	v_mul_f32_e64 v246, v232, -v120
	v_exp_f32_e32 v240, v239
	v_mul_f32_e32 v242, 0x3fb8aa3b, v241
	v_lshl_add_u64 v[140:141], v[140:141], 0, v[142:143]
	v_mul_f32_e32 v245, 0x3fb8aa3b, v244
	v_mul_f32_e32 v146, 0x3fb8aa3b, v246
	v_mul_f32_e64 v147, v232, -v121
	v_exp_f32_e32 v243, v242
	v_lshl_add_u64 v[140:141], v[140:141], 0, v[2:3]
	v_mul_f32_e64 v2, v232, -v128
	v_exp_f32_e32 v247, v245
	v_mul_f32_e32 v215, 0x3fb8aa3b, v147
	v_mul_f32_e64 v235, v232, -v122
	v_mul_f32_e64 v239, v232, -v123
	v_mul_f32_e32 v2, 0x3fb8aa3b, v2
	v_mul_f32_e64 v241, v232, -v117
	v_exp_f32_e32 v233, v215
	v_mul_f32_e32 v236, 0x3fb8aa3b, v235
	v_mul_f32_e64 v246, v232, -v119
	v_exp_f32_e32 v2, v2
	v_mul_f32_e32 v244, 0x3fb8aa3b, v241
	v_mul_f32_e64 v235, v231, -v114
	v_exp_f32_e32 v199, v236
	v_mul_f32_e32 v215, 0x3fb8aa3b, v108
	v_exp_f32_e32 v245, v244
	v_add_f32_e32 v2, 1.0, v2
	v_mul_f32_e32 v236, 0x3fb8aa3b, v235
	v_exp_f32_e32 v241, v215
	v_rcp_f32_e32 v128, v2
	v_add_f32_e32 v2, 1.0, v198
	v_exp_f32_e32 v198, v146
	v_mul_f32_e32 v146, 0x3fb8aa3b, v246
	v_mul_f32_e64 v246, v231, -v111
	v_rcp_f32_e32 v129, v2
	v_add_f32_e32 v2, 1.0, v234
	v_mul_f32_e32 v234, 0x3fb8aa3b, v239
	v_exp_f32_e32 v147, v146
	v_exp_f32_e32 v239, v236
	v_mul_f32_e32 v146, 0x3fb8aa3b, v246
	v_rcp_f32_e32 v130, v2
	v_add_f32_e32 v2, 1.0, v237
	v_mul_f32_e64 v237, v232, -v116
	v_rcp_f32_e32 v131, v2
	v_add_f32_e32 v2, 1.0, v238
	v_exp_f32_e32 v238, v234
	v_mul_f32_e64 v234, v231, -v115
	v_rcp_f32_e32 v124, v2
	v_add_f32_e32 v2, 1.0, v240
	v_mul_f32_e32 v240, 0x3fb8aa3b, v237
	v_mul_f32_e32 v237, 0x3fb8aa3b, v234
	v_rcp_f32_e32 v125, v2
	v_add_f32_e32 v2, 1.0, v243
	v_exp_f32_e32 v242, v240
	v_mul_f32_e64 v243, v231, -v113
	v_exp_f32_e32 v240, v237
	v_mul_f32_e64 v237, v231, -v106
	v_rcp_f32_e32 v126, v2
	v_add_f32_e32 v2, 1.0, v247
	v_mul_f32_e32 v247, 0x3fb8aa3b, v243
	v_exp_f32_e32 v243, v146
	v_mul_f32_e32 v215, 0x3fb8aa3b, v237
	v_mul_f32_e64 v237, v230, -v98
	v_rcp_f32_e32 v127, v2
	v_add_f32_e32 v2, 1.0, v198
	v_exp_f32_e32 v198, v247
	v_rcp_f32_e32 v120, v2
	v_add_f32_e32 v2, 1.0, v233
	v_mul_f32_e64 v233, v231, -v109
	v_rcp_f32_e32 v121, v2
	v_add_f32_e32 v2, 1.0, v199
	v_mul_f32_e32 v244, 0x3fb8aa3b, v233
	v_exp_f32_e32 v233, v215
	v_mul_f32_e32 v215, 0x3fb8aa3b, v237
	v_rcp_f32_e32 v122, v2
	v_add_f32_e32 v2, 1.0, v238
	v_mul_f32_e64 v238, v231, -v110
	v_exp_f32_e32 v199, v244
	v_mul_f32_e64 v244, v231, -v107
	v_rcp_f32_e32 v123, v2
	v_add_f32_e32 v2, 1.0, v242
	v_mul_f32_e32 v242, 0x3fb8aa3b, v238
	v_mul_f32_e64 v238, v231, -v101
	v_rcp_f32_e32 v116, v2
	v_add_f32_e32 v2, 1.0, v245
	v_exp_f32_e32 v245, v242
	v_mul_f32_e32 v246, 0x3fb8aa3b, v238
	v_mul_f32_e64 v238, v230, -v93
	v_rcp_f32_e32 v117, v2
	v_mul_f32_e64 v2, v232, -v118
	v_exp_f32_e32 v146, v246
	v_mul_f32_e32 v2, 0x3fb8aa3b, v2
	v_exp_f32_e32 v2, v2
	s_nop 0
	v_add_f32_e32 v2, 1.0, v2
	v_rcp_f32_e32 v118, v2
	v_add_f32_e32 v2, 1.0, v147
	v_mul_f32_e64 v147, v231, -v104
	v_rcp_f32_e32 v119, v2
	v_mul_f32_e64 v2, v231, -v112
	v_mul_f32_e32 v247, 0x3fb8aa3b, v147
	v_mul_f32_e64 v147, v231, -v103
	v_mul_f32_e32 v2, 0x3fb8aa3b, v2
	v_exp_f32_e32 v235, v247
	v_mul_f32_e32 v247, 0x3fb8aa3b, v147
	v_exp_f32_e32 v2, v2
	s_nop 0
	v_add_f32_e32 v2, 1.0, v2
	v_rcp_f32_e32 v112, v2
	v_add_f32_e32 v2, 1.0, v198
	v_mul_f32_e64 v198, v231, -v105
	v_rcp_f32_e32 v113, v2
	v_add_f32_e32 v2, 1.0, v239
	v_mul_f32_e32 v236, 0x3fb8aa3b, v198
	v_mul_f32_e32 v239, 0x3fb8aa3b, v244
	v_exp_f32_e32 v198, v247
	v_exp_f32_e32 v244, v215
	v_rcp_f32_e32 v114, v2
	v_add_f32_e32 v2, 1.0, v240
	v_exp_f32_e32 v234, v236
	v_mul_f32_e64 v240, v231, -v100
	v_mul_f32_e64 v236, v230, -v92
	v_mul_f32_e64 v247, v230, -v95
	v_rcp_f32_e32 v115, v2
	v_add_f32_e32 v2, 1.0, v241
	v_exp_f32_e32 v241, v239
	v_mul_f32_e64 v239, v230, -v99
	v_rcp_f32_e32 v108, v2
	v_add_f32_e32 v2, 1.0, v199
	v_mul_f32_e32 v199, 0x3fb8aa3b, v240
	v_mul_f32_e32 v240, 0x3fb8aa3b, v239
	v_rcp_f32_e32 v109, v2
	v_add_f32_e32 v2, 1.0, v245
	v_exp_f32_e32 v242, v199
	v_mul_f32_e64 v245, v230, -v97
	v_exp_f32_e32 v199, v240
	v_mul_f32_e64 v240, v230, -v90
	v_rcp_f32_e32 v110, v2
	v_add_f32_e32 v2, 1.0, v243
	v_mul_f32_e32 v243, 0x3fb8aa3b, v245
	v_mul_f32_e64 v245, v230, -v88
	v_rcp_f32_e32 v111, v2
	v_add_f32_e32 v2, 1.0, v235
	v_exp_f32_e32 v235, v243
	v_rcp_f32_e32 v104, v2
	v_add_f32_e32 v2, 1.0, v234
	v_mul_f32_e32 v234, 0x3fb8aa3b, v236
	v_mul_f32_e32 v236, 0x3fb8aa3b, v245
	v_mul_f32_e64 v245, v230, -v87
	v_rcp_f32_e32 v105, v2
	v_add_f32_e32 v2, 1.0, v233
	v_exp_f32_e32 v246, v234
	v_mul_f32_e32 v233, 0x3fb8aa3b, v238
	v_exp_f32_e32 v237, v236
	v_mul_f32_e32 v234, 0x3fb8aa3b, v240
	v_rcp_f32_e32 v106, v2
	v_add_f32_e32 v2, 1.0, v241
	v_exp_f32_e32 v241, v233
	v_mul_f32_e64 v233, v230, -v91
	v_exp_f32_e32 v238, v234
	v_mul_f32_e32 v236, 0x3fb8aa3b, v245
	v_rcp_f32_e32 v107, v2
	v_add_f32_e32 v2, 1.0, v242
	v_mul_f32_e64 v242, v230, -v94
	v_mul_f32_e64 v240, v229, -v82
	v_rcp_f32_e32 v100, v2
	v_add_f32_e32 v2, 1.0, v146
	v_mul_f32_e32 v146, 0x3fb8aa3b, v242
	v_mul_f32_e64 v242, v230, -v85
	v_mul_f32_e32 v234, 0x3fb8aa3b, v240
	v_rcp_f32_e32 v101, v2
	v_mul_f32_e64 v2, v231, -v102
	v_exp_f32_e32 v147, v146
	v_mul_f32_e32 v2, 0x3fb8aa3b, v2
	v_exp_f32_e32 v2, v2
	s_nop 0
	v_add_f32_e32 v2, 1.0, v2
	v_rcp_f32_e32 v102, v2
	v_add_f32_e32 v2, 1.0, v198
	v_mul_f32_e32 v198, 0x3fb8aa3b, v247
	v_mul_f32_e32 v247, 0x3fb8aa3b, v242
	v_mul_f32_e64 v242, v229, -v77
	v_rcp_f32_e32 v103, v2
	v_mul_f32_e64 v2, v230, -v96
	v_exp_f32_e32 v243, v198
	v_exp_f32_e32 v198, v247
	v_mul_f32_e32 v2, 0x3fb8aa3b, v2
	v_exp_f32_e32 v2, v2
	s_nop 0
	v_add_f32_e32 v2, 1.0, v2
	v_rcp_f32_e32 v96, v2
	v_add_f32_e32 v2, 1.0, v235
	v_mul_f32_e64 v235, v230, -v89
	v_rcp_f32_e32 v97, v2
	v_add_f32_e32 v2, 1.0, v244
	v_mul_f32_e32 v215, 0x3fb8aa3b, v235
	v_mul_f32_e32 v244, 0x3fb8aa3b, v233
	v_exp_f32_e32 v235, v236
	v_exp_f32_e32 v233, v234
	v_rcp_f32_e32 v98, v2
	v_add_f32_e32 v2, 1.0, v199
	v_exp_f32_e32 v239, v215
	v_mul_f32_e64 v199, v230, -v84
	v_mul_f32_e64 v215, v229, -v76
	v_mul_f32_e64 v236, v229, -v79
	v_rcp_f32_e32 v99, v2
	v_add_f32_e32 v2, 1.0, v246
	v_exp_f32_e32 v246, v244
	v_mul_f32_e64 v244, v229, -v83
	v_rcp_f32_e32 v92, v2
	v_add_f32_e32 v2, 1.0, v241
	v_mul_f32_e32 v241, 0x3fb8aa3b, v199
	v_mul_f32_e32 v199, 0x3fb8aa3b, v244
	v_rcp_f32_e32 v93, v2
	v_add_f32_e32 v2, 1.0, v147
	v_exp_f32_e32 v146, v241
	v_mul_f32_e64 v147, v229, -v81
	v_exp_f32_e32 v241, v199
	v_mul_f32_e64 v199, v229, -v74
	v_rcp_f32_e32 v94, v2
	v_add_f32_e32 v2, 1.0, v243
	v_mul_f32_e32 v243, 0x3fb8aa3b, v147
	v_mul_f32_e64 v147, v229, -v72
	v_rcp_f32_e32 v95, v2
	v_add_f32_e32 v2, 1.0, v237
	v_exp_f32_e32 v237, v243
	v_rcp_f32_e32 v88, v2
	v_add_f32_e32 v2, 1.0, v239
	v_mul_f32_e32 v239, 0x3fb8aa3b, v215
	v_mul_f32_e32 v215, 0x3fb8aa3b, v147
	v_mul_f32_e64 v147, v229, -v71
	v_rcp_f32_e32 v89, v2
	v_add_f32_e32 v2, 1.0, v238
	v_exp_f32_e32 v247, v239
	v_mul_f32_e32 v238, 0x3fb8aa3b, v242
	v_exp_f32_e32 v240, v215
	v_mul_f32_e32 v239, 0x3fb8aa3b, v199
	v_rcp_f32_e32 v90, v2
	v_add_f32_e32 v2, 1.0, v246
	v_exp_f32_e32 v246, v238
	v_mul_f32_e64 v238, v229, -v75
	v_exp_f32_e32 v242, v239
	v_mul_f32_e32 v215, 0x3fb8aa3b, v147
	v_rcp_f32_e32 v91, v2
	v_add_f32_e32 v2, 1.0, v146
	v_mul_f32_e64 v146, v229, -v78
	v_mul_f32_e64 v199, v228, -v66
	v_rcp_f32_e32 v84, v2
	v_add_f32_e32 v2, 1.0, v198
	v_mul_f32_e32 v198, 0x3fb8aa3b, v146
	v_mul_f32_e64 v146, v229, -v69
	v_mul_f32_e32 v239, 0x3fb8aa3b, v199
	v_rcp_f32_e32 v85, v2
	v_mul_f32_e64 v2, v230, -v86
	v_exp_f32_e32 v245, v198
	v_mul_f32_e32 v2, 0x3fb8aa3b, v2
	v_exp_f32_e32 v2, v2
	s_nop 0
	v_add_f32_e32 v2, 1.0, v2
	v_rcp_f32_e32 v86, v2
	v_add_f32_e32 v2, 1.0, v235
	v_mul_f32_e32 v235, 0x3fb8aa3b, v236
	v_mul_f32_e32 v236, 0x3fb8aa3b, v146
	v_mul_f32_e64 v146, v228, -v61
	v_rcp_f32_e32 v87, v2
	v_mul_f32_e64 v2, v229, -v80
	v_exp_f32_e32 v243, v235
	v_exp_f32_e32 v235, v236
	v_mul_f32_e32 v2, 0x3fb8aa3b, v2
	v_exp_f32_e32 v2, v2
	s_nop 0
	v_add_f32_e32 v2, 1.0, v2
	v_rcp_f32_e32 v80, v2
	v_add_f32_e32 v2, 1.0, v237
	v_mul_f32_e64 v237, v229, -v73
	v_rcp_f32_e32 v81, v2
	v_add_f32_e32 v2, 1.0, v233
	v_mul_f32_e32 v234, 0x3fb8aa3b, v237
	v_mul_f32_e32 v233, 0x3fb8aa3b, v238
	v_exp_f32_e32 v237, v215
	v_exp_f32_e32 v238, v239
	v_rcp_f32_e32 v82, v2
	v_add_f32_e32 v2, 1.0, v241
	v_exp_f32_e32 v244, v234
	v_mul_f32_e64 v241, v229, -v68
	v_mul_f32_e64 v234, v228, -v60
	v_mul_f32_e64 v215, v228, -v63
	v_rcp_f32_e32 v83, v2
	v_add_f32_e32 v2, 1.0, v247
	v_exp_f32_e32 v247, v233
	v_mul_f32_e64 v233, v228, -v67
	v_rcp_f32_e32 v76, v2
	v_add_f32_e32 v2, 1.0, v246
	v_mul_f32_e32 v246, 0x3fb8aa3b, v241
	v_mul_f32_e32 v241, 0x3fb8aa3b, v233
	v_rcp_f32_e32 v77, v2
	v_add_f32_e32 v2, 1.0, v245
	v_exp_f32_e32 v198, v246
	v_mul_f32_e64 v245, v228, -v65
	v_exp_f32_e32 v246, v241
	v_mul_f32_e64 v241, v228, -v58
	v_rcp_f32_e32 v78, v2
	v_add_f32_e32 v2, 1.0, v243
	v_mul_f32_e32 v243, 0x3fb8aa3b, v245
	v_mul_f32_e64 v245, v228, -v56
	v_rcp_f32_e32 v79, v2
	v_add_f32_e32 v2, 1.0, v240
	v_exp_f32_e32 v240, v243
	v_rcp_f32_e32 v72, v2
	v_add_f32_e32 v2, 1.0, v244
	v_mul_f32_e32 v244, 0x3fb8aa3b, v234
	v_mul_f32_e32 v234, 0x3fb8aa3b, v245
	v_mul_f32_e64 v245, v228, -v55
	v_rcp_f32_e32 v73, v2
	v_add_f32_e32 v2, 1.0, v242
	v_exp_f32_e32 v236, v244
	v_mul_f32_e32 v242, 0x3fb8aa3b, v146
	v_exp_f32_e32 v199, v234
	v_mul_f32_e32 v244, 0x3fb8aa3b, v241
	v_rcp_f32_e32 v74, v2
	v_add_f32_e32 v2, 1.0, v247
	v_exp_f32_e32 v247, v242
	v_mul_f32_e64 v242, v228, -v59
	v_exp_f32_e32 v146, v244
	v_mul_f32_e32 v234, 0x3fb8aa3b, v245
	v_rcp_f32_e32 v75, v2
	v_add_f32_e32 v2, 1.0, v198
	v_mul_f32_e64 v198, v228, -v62
	v_mul_f32_e64 v241, v227, -v50
	v_rcp_f32_e32 v68, v2
	v_add_f32_e32 v2, 1.0, v235
	v_mul_f32_e32 v235, 0x3fb8aa3b, v198
	v_mul_f32_e64 v198, v228, -v53
	v_mul_f32_e32 v244, 0x3fb8aa3b, v241
	v_rcp_f32_e32 v69, v2
	v_mul_f32_e64 v2, v229, -v70
	v_exp_f32_e32 v147, v235
	v_mul_f32_e32 v2, 0x3fb8aa3b, v2
	v_exp_f32_e32 v2, v2
	s_nop 0
	v_add_f32_e32 v2, 1.0, v2
	v_rcp_f32_e32 v70, v2
	v_add_f32_e32 v2, 1.0, v237
	v_mul_f32_e32 v237, 0x3fb8aa3b, v215
	v_mul_f32_e32 v215, 0x3fb8aa3b, v198
	v_mul_f32_e64 v198, v227, -v45
	v_rcp_f32_e32 v71, v2
	v_mul_f32_e64 v2, v228, -v64
	v_exp_f32_e32 v243, v237
	v_exp_f32_e32 v237, v215
	v_mul_f32_e32 v2, 0x3fb8aa3b, v2
	v_exp_f32_e32 v2, v2
	s_nop 0
	v_add_f32_e32 v2, 1.0, v2
	v_rcp_f32_e32 v64, v2
	v_add_f32_e32 v2, 1.0, v240
	v_mul_f32_e64 v240, v228, -v57
	v_rcp_f32_e32 v65, v2
	v_add_f32_e32 v2, 1.0, v238
	v_mul_f32_e32 v239, 0x3fb8aa3b, v240
	v_mul_f32_e32 v238, 0x3fb8aa3b, v242
	v_exp_f32_e32 v240, v234
	v_exp_f32_e32 v242, v244
	v_rcp_f32_e32 v66, v2
	v_add_f32_e32 v2, 1.0, v246
	v_exp_f32_e32 v233, v239
	v_mul_f32_e64 v246, v228, -v52
	v_mul_f32_e64 v239, v227, -v44
	v_mul_f32_e64 v234, v227, -v47
	v_rcp_f32_e32 v67, v2
	v_add_f32_e32 v2, 1.0, v236
	v_exp_f32_e32 v236, v238
	v_mul_f32_e64 v238, v227, -v51
	v_rcp_f32_e32 v60, v2
	v_add_f32_e32 v2, 1.0, v247
	v_mul_f32_e32 v247, 0x3fb8aa3b, v246
	v_mul_f32_e32 v246, 0x3fb8aa3b, v238
	v_rcp_f32_e32 v61, v2
	v_add_f32_e32 v2, 1.0, v147
	v_exp_f32_e32 v235, v247
	v_mul_f32_e64 v147, v227, -v49
	v_exp_f32_e32 v247, v246
	v_mul_f32_e64 v246, v227, -v42
	v_rcp_f32_e32 v62, v2
	v_add_f32_e32 v2, 1.0, v243
	v_mul_f32_e32 v243, 0x3fb8aa3b, v147
	v_mul_f32_e64 v147, v227, -v40
	v_rcp_f32_e32 v63, v2
	v_add_f32_e32 v2, 1.0, v199
	v_exp_f32_e32 v199, v243
	v_rcp_f32_e32 v56, v2
	v_add_f32_e32 v2, 1.0, v233
	v_mul_f32_e32 v233, 0x3fb8aa3b, v239
	v_mul_f32_e32 v239, 0x3fb8aa3b, v147
	v_mul_f32_e64 v147, v227, -v39
	v_rcp_f32_e32 v57, v2
	v_add_f32_e32 v2, 1.0, v146
	v_exp_f32_e32 v215, v233
	v_mul_f32_e32 v146, 0x3fb8aa3b, v198
	v_exp_f32_e32 v241, v239
	v_mul_f32_e32 v233, 0x3fb8aa3b, v246
	v_rcp_f32_e32 v58, v2
	v_add_f32_e32 v2, 1.0, v236
	v_exp_f32_e32 v236, v146
	v_mul_f32_e64 v146, v227, -v43
	v_exp_f32_e32 v198, v233
	v_rcp_f32_e32 v59, v2
	v_add_f32_e32 v2, 1.0, v235
	v_mul_f32_e64 v235, v227, -v46
	v_rcp_f32_e32 v52, v2
	v_add_f32_e32 v2, 1.0, v237
	v_mul_f32_e32 v237, 0x3fb8aa3b, v235
	v_mul_f32_e64 v235, v227, -v37
	v_rcp_f32_e32 v53, v2
	v_mul_f32_e64 v2, v228, -v54
	v_exp_f32_e32 v245, v237
	v_mul_f32_e32 v2, 0x3fb8aa3b, v2
	v_exp_f32_e32 v2, v2
	s_nop 0
	v_add_f32_e32 v2, 1.0, v2
	v_rcp_f32_e32 v54, v2
	v_add_f32_e32 v2, 1.0, v240
	v_mul_f32_e32 v240, 0x3fb8aa3b, v234
	v_mul_f32_e32 v234, 0x3fb8aa3b, v235
	v_rcp_f32_e32 v55, v2
	v_mul_f32_e64 v2, v227, -v48
	v_exp_f32_e32 v243, v240
	v_exp_f32_e32 v240, v234
	v_mul_f32_e32 v2, 0x3fb8aa3b, v2
	v_exp_f32_e32 v2, v2
	s_nop 0
	v_add_f32_e32 v2, 1.0, v2
	v_rcp_f32_e32 v48, v2
	v_add_f32_e32 v2, 1.0, v199
	v_mul_f32_e64 v199, v227, -v41
	v_rcp_f32_e32 v49, v2
	v_add_f32_e32 v2, 1.0, v242
	v_mul_f32_e32 v244, 0x3fb8aa3b, v199
	v_mul_f32_e32 v242, 0x3fb8aa3b, v146
	v_rcp_f32_e32 v50, v2
	v_add_f32_e32 v2, 1.0, v247
	v_exp_f32_e32 v238, v244
	v_mul_f32_e64 v247, v227, -v36
	v_rcp_f32_e32 v51, v2
	v_add_f32_e32 v2, 1.0, v215
	v_exp_f32_e32 v215, v242
	v_rcp_f32_e32 v44, v2
	v_add_f32_e32 v2, 1.0, v236
	v_mul_f32_e32 v236, 0x3fb8aa3b, v247
	v_rcp_f32_e32 v45, v2
	v_add_f32_e32 v2, 1.0, v245
	v_exp_f32_e32 v237, v236
	v_rcp_f32_e32 v46, v2
	v_add_f32_e32 v2, 1.0, v243
	v_rcp_f32_e32 v47, v2
	v_add_f32_e32 v2, 1.0, v241
	v_rcp_f32_e32 v40, v2
	v_add_f32_e32 v2, 1.0, v238
	v_rcp_f32_e32 v41, v2
	v_add_f32_e32 v2, 1.0, v198
	v_rcp_f32_e32 v42, v2
	v_add_f32_e32 v2, 1.0, v215
	v_rcp_f32_e32 v43, v2
	v_add_f32_e32 v2, 1.0, v237
	v_rcp_f32_e32 v36, v2
	v_add_f32_e32 v2, 1.0, v240
	v_rcp_f32_e32 v37, v2
	v_mul_f32_e64 v2, v227, -v38
	v_mul_f32_e32 v38, 0x3fb8aa3b, v147
	v_mul_f32_e32 v2, 0x3fb8aa3b, v2
	v_exp_f32_e32 v39, v38
	v_exp_f32_e32 v2, v2
	s_nop 0
	v_add_co_u32_e32 v142, vcc, s12, v140
	v_mul_f32_e64 v145, v226, -v32
	v_add_f32_e32 v143, 1.0, v2
	v_add_f32_e32 v144, 1.0, v39
	v_mul_f32_e64 v147, v226, -v33
	v_mul_f32_e32 v146, 0x3fb8aa3b, v145
	v_rcp_f32_e32 v38, v143
	v_rcp_f32_e32 v39, v144
	v_mul_f32_e32 v32, 0x3fb8aa3b, v147
	v_exp_f32_e32 v2, v146
	s_nop 0
	v_addc_co_u32_e32 v143, vcc, 0, v141, vcc
	v_exp_f32_e32 v33, v32
	v_add_co_u32_e32 v196, vcc, s5, v140
	v_add_f32_e32 v2, 1.0, v2
	s_nop 0
	v_addc_co_u32_e32 v197, vcc, 0, v141, vcc
	v_add_co_u32_e32 v198, vcc, s4, v140
	v_rcp_f32_e32 v32, v2
	s_nop 0
	v_addc_co_u32_e32 v199, vcc, 0, v141, vcc
	global_load_dwordx2 v[146:147], v[140:141], off
	global_load_dwordx2 v[144:145], v[142:143], off
	s_nop 0
	global_load_dwordx2 v[142:143], v[196:197], off
	global_load_dwordx2 v[140:141], v[198:199], off
	v_lshlrev_b32_e32 v196, 16, v222
	v_and_b32_e32 v197, 0xffff0000, v222
	v_mul_f32_e64 v199, v226, -v34
	v_mul_f32_e64 v229, v226, -v35
	v_mul_f32_e64 v231, v226, -v28
	v_mul_f32_e64 v234, v226, -v29
	v_pk_fma_f32 v[128:129], v[128:129], v[196:197], 0 op_sel_hi:[1,1,0]
	v_lshlrev_b32_e32 v196, 16, v220
	v_and_b32_e32 v197, 0xffff0000, v220
	v_mul_f32_e32 v227, 0x3fb8aa3b, v199
	v_mul_f32_e32 v230, 0x3fb8aa3b, v229
	v_mul_f32_e32 v233, 0x3fb8aa3b, v231
	v_mul_f32_e32 v236, 0x3fb8aa3b, v234
	v_pk_fma_f32 v[124:125], v[124:125], v[196:197], v[128:129]
	v_lshlrev_b32_e32 v128, 16, v218
	v_and_b32_e32 v129, 0xffff0000, v218
	v_exp_f32_e32 v228, v227
	v_exp_f32_e32 v232, v230
	v_exp_f32_e32 v235, v233
	v_ashrrev_i32_e32 v215, 31, v214
	v_pk_fma_f32 v[120:121], v[120:121], v[128:129], v[124:125]
	v_lshlrev_b32_e32 v124, 16, v216
	v_and_b32_e32 v125, 0xffff0000, v216
	v_exp_f32_e32 v237, v236
	v_add_f32_e32 v198, 1.0, v33
	v_add_f32_e32 v238, 1.0, v228
	v_add_f32_e32 v239, 1.0, v232
	v_pk_fma_f32 v[116:117], v[116:117], v[124:125], v[120:121]
	v_lshlrev_b32_e32 v120, 16, v223
	v_and_b32_e32 v121, 0xffff0000, v223
	v_lshlrev_b32_e32 v124, 16, v221
	v_and_b32_e32 v125, 0xffff0000, v221
	v_add_f32_e32 v240, 1.0, v235
	v_rcp_f32_e32 v33, v198
	v_pk_fma_f32 v[120:121], v[130:131], v[120:121], 0 op_sel_hi:[1,1,0]
	v_rcp_f32_e32 v34, v238
	v_rcp_f32_e32 v35, v239
	v_rcp_f32_e32 v28, v240
	v_add_f32_e32 v2, 1.0, v237
	v_pk_fma_f32 v[120:121], v[126:127], v[124:125], v[120:121]
	v_lshlrev_b32_e32 v124, 16, v219
	v_and_b32_e32 v125, 0xffff0000, v219
	v_mul_f32_e64 v29, v226, -v30
	v_pk_fma_f32 v[120:121], v[122:123], v[124:125], v[120:121]
	v_lshlrev_b32_e32 v122, 16, v217
	v_and_b32_e32 v123, 0xffff0000, v217
	v_pk_fma_f32 v[118:119], v[118:119], v[122:123], v[120:121]
	v_cvt_pk_bf16_f32 v120, v116, v117
	v_lshlrev_b64 v[116:117], 11, v[212:213]
	v_cvt_pk_bf16_f32 v121, v118, v119
	v_lshlrev_b64 v[118:119], 1, v[214:215]
	v_lshl_add_u64 v[116:117], s[14:15], 0, v[116:117]
	v_lshl_add_u64 v[116:117], v[116:117], 0, v[118:119]
	global_store_dwordx2 v[116:117], v[120:121], off
	v_mul_f32_e64 v124, v226, -v31
	v_mul_f32_e64 v126, v226, -v24
	v_lshlrev_b32_e32 v120, 16, v204
	v_and_b32_e32 v121, 0xffff0000, v204
	v_mul_f32_e32 v122, 0x3fb8aa3b, v29
	v_mul_f32_e32 v125, 0x3fb8aa3b, v124
	v_mul_f32_e32 v128, 0x3fb8aa3b, v126
	v_mul_f32_e64 v129, v226, -v25
	v_pk_fma_f32 v[112:113], v[112:113], v[120:121], 0 op_sel_hi:[1,1,0]
	v_lshlrev_b32_e32 v120, 16, v210
	v_and_b32_e32 v121, 0xffff0000, v210
	v_exp_f32_e32 v123, v122
	v_exp_f32_e32 v127, v125
	v_exp_f32_e32 v130, v128
	v_mul_f32_e32 v131, 0x3fb8aa3b, v129
	v_pk_fma_f32 v[108:109], v[108:109], v[120:121], v[112:113]
	v_lshlrev_b32_e32 v112, 16, v208
	v_and_b32_e32 v113, 0xffff0000, v208
	v_mul_f32_e64 v212, v226, -v26
	v_exp_f32_e32 v196, v131
	v_add_f32_e32 v197, 1.0, v123
	v_add_f32_e32 v198, 1.0, v127
	v_pk_fma_f32 v[104:105], v[104:105], v[112:113], v[108:109]
	v_lshlrev_b32_e32 v108, 16, v206
	v_and_b32_e32 v109, 0xffff0000, v206
	v_add_f32_e32 v199, 1.0, v130
	v_mul_f32_e32 v213, 0x3fb8aa3b, v212
	v_rcp_f32_e32 v29, v2
	v_rcp_f32_e32 v30, v197
	v_pk_fma_f32 v[100:101], v[100:101], v[108:109], v[104:105]
	v_lshlrev_b32_e32 v104, 16, v205
	v_and_b32_e32 v105, 0xffff0000, v205
	v_lshlrev_b32_e32 v108, 16, v211
	v_and_b32_e32 v109, 0xffff0000, v211
	v_cvt_pk_bf16_f32 v100, v100, v101
	v_rcp_f32_e32 v31, v198
	v_pk_fma_f32 v[104:105], v[114:115], v[104:105], 0 op_sel_hi:[1,1,0]
	v_rcp_f32_e32 v24, v199
	v_add_f32_e32 v2, 1.0, v196
	v_exp_f32_e32 v26, v213
	v_mul_f32_e64 v25, v226, -v27
	v_pk_fma_f32 v[104:105], v[110:111], v[108:109], v[104:105]
	v_lshlrev_b32_e32 v108, 16, v209
	v_and_b32_e32 v109, 0xffff0000, v209
	v_pk_fma_f32 v[104:105], v[106:107], v[108:109], v[104:105]
	v_lshlrev_b32_e32 v106, 16, v207
	v_and_b32_e32 v107, 0xffff0000, v207
	v_pk_fma_f32 v[102:103], v[102:103], v[106:107], v[104:105]
	v_cvt_pk_bf16_f32 v101, v102, v103
	v_lshlrev_b64 v[102:103], 11, v[194:195]
	v_lshl_add_u64 v[102:103], s[14:15], 0, v[102:103]
	v_lshl_add_u64 v[102:103], v[102:103], 0, v[118:119]
	global_store_dwordx2 v[102:103], v[100:101], off
	v_mul_f32_e64 v106, v226, -v21
	v_mul_f32_e64 v114, v226, -v22
	v_lshlrev_b32_e32 v100, 16, v192
	v_and_b32_e32 v101, 0xffff0000, v192
	v_mul_f32_e64 v103, v226, -v20
	v_mul_f32_e32 v102, 0x3fb8aa3b, v25
	v_mul_f32_e32 v108, 0x3fb8aa3b, v106
	v_mul_f32_e64 v120, v226, -v23
	v_pk_fma_f32 v[96:97], v[96:97], v[100:101], 0 op_sel_hi:[1,1,0]
	v_lshlrev_b32_e32 v100, 16, v190
	v_and_b32_e32 v101, 0xffff0000, v190
	v_mul_f32_e32 v105, 0x3fb8aa3b, v103
	v_exp_f32_e32 v104, v102
	v_exp_f32_e32 v109, v108
	v_add_f32_e32 v110, 1.0, v26
	v_pk_fma_f32 v[92:93], v[92:93], v[100:101], v[96:97]
	v_lshlrev_b32_e32 v96, 16, v188
	v_and_b32_e32 v97, 0xffff0000, v188
	v_exp_f32_e32 v107, v105
	v_add_f32_e32 v111, 1.0, v104
	v_add_f32_e32 v113, 1.0, v109
	v_mul_f32_e32 v115, 0x3fb8aa3b, v114
	v_pk_fma_f32 v[88:89], v[88:89], v[96:97], v[92:93]
	v_lshlrev_b32_e32 v92, 16, v186
	v_and_b32_e32 v93, 0xffff0000, v186
	v_add_f32_e32 v112, 1.0, v107
	v_mul_f32_e32 v22, 0x3fb8aa3b, v120
	v_rcp_f32_e32 v25, v2
	v_rcp_f32_e32 v26, v110
	v_pk_fma_f32 v[84:85], v[84:85], v[92:93], v[88:89]
	v_lshlrev_b32_e32 v88, 16, v193
	v_and_b32_e32 v89, 0xffff0000, v193
	v_lshlrev_b32_e32 v92, 16, v191
	v_and_b32_e32 v93, 0xffff0000, v191
	v_cvt_pk_bf16_f32 v84, v84, v85
	v_rcp_f32_e32 v27, v111
	v_pk_fma_f32 v[88:89], v[98:99], v[88:89], 0 op_sel_hi:[1,1,0]
	v_rcp_f32_e32 v20, v112
	v_rcp_f32_e32 v21, v113
	v_exp_f32_e32 v2, v115
	v_exp_f32_e32 v23, v22
	v_pk_fma_f32 v[88:89], v[94:95], v[92:93], v[88:89]
	v_lshlrev_b32_e32 v92, 16, v189
	v_and_b32_e32 v93, 0xffff0000, v189
	v_pk_fma_f32 v[88:89], v[90:91], v[92:93], v[88:89]
	v_lshlrev_b32_e32 v90, 16, v187
	v_and_b32_e32 v91, 0xffff0000, v187
	v_pk_fma_f32 v[86:87], v[86:87], v[90:91], v[88:89]
	v_cvt_pk_bf16_f32 v85, v86, v87
	v_lshlrev_b64 v[86:87], 11, v[184:185]
	v_lshl_add_u64 v[86:87], s[14:15], 0, v[86:87]
	v_lshl_add_u64 v[86:87], v[86:87], 0, v[118:119]
	global_store_dwordx2 v[86:87], v[84:85], off
	v_lshlrev_b32_e32 v84, 16, v180
	v_and_b32_e32 v85, 0xffff0000, v180
	v_pk_fma_f32 v[80:81], v[80:81], v[84:85], 0 op_sel_hi:[1,1,0]
	v_lshlrev_b32_e32 v84, 16, v178
	v_and_b32_e32 v85, 0xffff0000, v178
	v_pk_fma_f32 v[76:77], v[76:77], v[84:85], v[80:81]
	v_lshlrev_b32_e32 v80, 16, v176
	v_and_b32_e32 v81, 0xffff0000, v176
	v_add_f32_e32 v2, 1.0, v2
	v_pk_fma_f32 v[72:73], v[72:73], v[80:81], v[76:77]
	v_lshlrev_b32_e32 v76, 16, v182
	v_and_b32_e32 v77, 0xffff0000, v182
	v_rcp_f32_e32 v22, v2
	v_add_f32_e32 v2, 1.0, v23
	v_pk_fma_f32 v[68:69], v[68:69], v[76:77], v[72:73]
	v_lshlrev_b32_e32 v72, 16, v181
	v_and_b32_e32 v73, 0xffff0000, v181
	v_rcp_f32_e32 v23, v2
	s_waitcnt vmcnt(7)
	v_pk_fma_f32 v[72:73], v[82:83], v[72:73], 0 op_sel_hi:[1,1,0]
	v_lshlrev_b32_e32 v76, 16, v179
	v_and_b32_e32 v77, 0xffff0000, v179
	v_mul_f32_e64 v80, v225, -v16
	v_mul_f32_e64 v84, v225, -v17
	v_cvt_pk_bf16_f32 v68, v68, v69
	v_mul_f32_e64 v17, v225, -v18
	v_pk_fma_f32 v[72:73], v[78:79], v[76:77], v[72:73]
	v_lshlrev_b32_e32 v76, 16, v177
	v_and_b32_e32 v77, 0xffff0000, v177
	v_mul_f32_e32 v81, 0x3fb8aa3b, v80
	v_mul_f32_e32 v86, 0x3fb8aa3b, v84
	v_pk_fma_f32 v[72:73], v[74:75], v[76:77], v[72:73]
	v_lshlrev_b32_e32 v74, 16, v183
	v_and_b32_e32 v75, 0xffff0000, v183
	v_exp_f32_e32 v85, v81
	v_exp_f32_e32 v87, v86
	v_pk_fma_f32 v[70:71], v[70:71], v[74:75], v[72:73]
	v_add_f32_e32 v88, 1.0, v85
	v_add_f32_e32 v2, 1.0, v87
	v_cvt_pk_bf16_f32 v69, v70, v71
	v_lshlrev_b64 v[70:71], 11, v[174:175]
	v_rcp_f32_e32 v16, v88
	v_lshl_add_u64 v[70:71], s[14:15], 0, v[70:71]
	v_lshl_add_u64 v[70:71], v[70:71], 0, v[118:119]
	global_store_dwordx2 v[70:71], v[68:69], off
	v_mul_f32_e64 v72, v225, -v19
	v_mul_f32_e64 v74, v225, -v12
	v_lshlrev_b32_e32 v68, 16, v170
	v_and_b32_e32 v69, 0xffff0000, v170
	v_mul_f32_e32 v70, 0x3fb8aa3b, v17
	v_mul_f32_e32 v73, 0x3fb8aa3b, v72
	v_mul_f32_e32 v76, 0x3fb8aa3b, v74
	v_mul_f32_e64 v77, v225, -v13
	v_pk_fma_f32 v[64:65], v[64:65], v[68:69], 0 op_sel_hi:[1,1,0]
	v_lshlrev_b32_e32 v68, 16, v168
	v_and_b32_e32 v69, 0xffff0000, v168
	v_exp_f32_e32 v71, v70
	v_exp_f32_e32 v75, v73
	v_exp_f32_e32 v78, v76
	v_mul_f32_e32 v79, 0x3fb8aa3b, v77
	v_pk_fma_f32 v[60:61], v[60:61], v[68:69], v[64:65]
	v_lshlrev_b32_e32 v64, 16, v166
	v_and_b32_e32 v65, 0xffff0000, v166
	v_mul_f32_e64 v84, v225, -v14
	v_exp_f32_e32 v80, v79
	v_add_f32_e32 v81, 1.0, v71
	v_add_f32_e32 v82, 1.0, v75
	v_pk_fma_f32 v[56:57], v[56:57], v[64:65], v[60:61]
	v_lshlrev_b32_e32 v60, 16, v172
	v_and_b32_e32 v61, 0xffff0000, v172
	v_add_f32_e32 v83, 1.0, v78
	v_mul_f32_e32 v85, 0x3fb8aa3b, v84
	v_rcp_f32_e32 v17, v2
	v_rcp_f32_e32 v18, v81
	v_pk_fma_f32 v[52:53], v[52:53], v[60:61], v[56:57]
	v_lshlrev_b32_e32 v56, 16, v171
	v_and_b32_e32 v57, 0xffff0000, v171
	v_lshlrev_b32_e32 v60, 16, v169
	v_and_b32_e32 v61, 0xffff0000, v169
	v_cvt_pk_bf16_f32 v52, v52, v53
	v_rcp_f32_e32 v19, v82
	v_pk_fma_f32 v[56:57], v[66:67], v[56:57], 0 op_sel_hi:[1,1,0]
	v_rcp_f32_e32 v12, v83
	v_add_f32_e32 v2, 1.0, v80
	v_exp_f32_e32 v14, v85
	v_mul_f32_e64 v13, v225, -v15
	v_pk_fma_f32 v[56:57], v[62:63], v[60:61], v[56:57]
	v_lshlrev_b32_e32 v60, 16, v167
	v_and_b32_e32 v61, 0xffff0000, v167
	v_pk_fma_f32 v[56:57], v[58:59], v[60:61], v[56:57]
	v_lshlrev_b32_e32 v58, 16, v173
	v_and_b32_e32 v59, 0xffff0000, v173
	v_pk_fma_f32 v[54:55], v[54:55], v[58:59], v[56:57]
	v_cvt_pk_bf16_f32 v53, v54, v55
	v_lshlrev_b64 v[54:55], 11, v[164:165]
	v_lshl_add_u64 v[54:55], s[14:15], 0, v[54:55]
	v_lshl_add_u64 v[54:55], v[54:55], 0, v[118:119]
	global_store_dwordx2 v[54:55], v[52:53], off
	v_lshlrev_b32_e32 v52, 16, v158
	v_and_b32_e32 v53, 0xffff0000, v158
	v_mul_f32_e32 v13, 0x3fb8aa3b, v13
	v_mul_f32_e64 v8, v225, -v8
	v_pk_fma_f32 v[48:49], v[48:49], v[52:53], 0 op_sel_hi:[1,1,0]
	v_lshlrev_b32_e32 v52, 16, v156
	v_and_b32_e32 v53, 0xffff0000, v156
	v_exp_f32_e32 v15, v13
	v_mul_f32_e32 v8, 0x3fb8aa3b, v8
	v_mul_f32_e64 v9, v225, -v9
	v_pk_fma_f32 v[44:45], v[44:45], v[52:53], v[48:49]
	v_lshlrev_b32_e32 v48, 16, v162
	v_and_b32_e32 v49, 0xffff0000, v162
	v_exp_f32_e32 v8, v8
	v_mul_f32_e32 v9, 0x3fb8aa3b, v9
	v_pk_fma_f32 v[40:41], v[40:41], v[48:49], v[44:45]
	v_lshlrev_b32_e32 v44, 16, v160
	v_and_b32_e32 v45, 0xffff0000, v160
	v_exp_f32_e32 v9, v9
	v_pk_fma_f32 v[36:37], v[36:37], v[44:45], v[40:41]
	v_lshlrev_b32_e32 v40, 16, v159
	v_and_b32_e32 v41, 0xffff0000, v159
	v_rcp_f32_e32 v13, v2
	v_add_f32_e32 v2, 1.0, v14
	v_pk_fma_f32 v[40:41], v[50:51], v[40:41], 0 op_sel_hi:[1,1,0]
	v_lshlrev_b32_e32 v44, 16, v157
	v_and_b32_e32 v45, 0xffff0000, v157
	v_rcp_f32_e32 v14, v2
	v_add_f32_e32 v2, 1.0, v15
	v_pk_fma_f32 v[40:41], v[46:47], v[44:45], v[40:41]
	v_lshlrev_b32_e32 v44, 16, v163
	v_and_b32_e32 v45, 0xffff0000, v163
	v_rcp_f32_e32 v15, v2
	v_add_f32_e32 v2, 1.0, v8
	v_pk_fma_f32 v[40:41], v[42:43], v[44:45], v[40:41]
	v_lshlrev_b32_e32 v42, 16, v161
	v_and_b32_e32 v43, 0xffff0000, v161
	v_rcp_f32_e32 v8, v2
	v_add_f32_e32 v2, 1.0, v9
	v_mul_f32_e64 v9, v225, -v10
	v_pk_fma_f32 v[38:39], v[38:39], v[42:43], v[40:41]
	s_mov_b32 s4, 0x48000
	v_mul_f32_e32 v9, 0x3fb8aa3b, v9
	v_cvt_pk_bf16_f32 v36, v36, v37
	v_cvt_pk_bf16_f32 v37, v38, v39
	v_add_co_u32_e32 v38, vcc, s4, v116
	v_exp_f32_e32 v10, v9
	v_mul_f32_e64 v9, v225, -v11
	v_addc_co_u32_e32 v39, vcc, 0, v117, vcc
	v_mul_f32_e32 v9, 0x3fb8aa3b, v9
	v_mul_f32_e64 v4, v225, -v4
	global_store_dwordx2 v[38:39], v[36:37], off
	v_lshlrev_b32_e32 v36, 16, v148
	v_and_b32_e32 v37, 0xffff0000, v148
	v_exp_f32_e32 v11, v9
	v_mul_f32_e32 v4, 0x3fb8aa3b, v4
	v_mul_f32_e64 v5, v225, -v5
	v_pk_fma_f32 v[32:33], v[32:33], v[36:37], 0 op_sel_hi:[1,1,0]
	v_lshlrev_b32_e32 v36, 16, v154
	v_and_b32_e32 v37, 0xffff0000, v154
	v_exp_f32_e32 v4, v4
	v_mul_f32_e32 v5, 0x3fb8aa3b, v5
	v_pk_fma_f32 v[28:29], v[28:29], v[36:37], v[32:33]
	v_lshlrev_b32_e32 v32, 16, v152
	v_and_b32_e32 v33, 0xffff0000, v152
	v_exp_f32_e32 v5, v5
	v_pk_fma_f32 v[24:25], v[24:25], v[32:33], v[28:29]
	v_lshlrev_b32_e32 v28, 16, v150
	v_and_b32_e32 v29, 0xffff0000, v150
	v_rcp_f32_e32 v9, v2
	v_add_f32_e32 v2, 1.0, v10
	v_pk_fma_f32 v[20:21], v[20:21], v[28:29], v[24:25]
	v_lshlrev_b32_e32 v24, 16, v149
	v_and_b32_e32 v25, 0xffff0000, v149
	v_rcp_f32_e32 v10, v2
	v_add_f32_e32 v2, 1.0, v11
	v_pk_fma_f32 v[24:25], v[34:35], v[24:25], 0 op_sel_hi:[1,1,0]
	v_lshlrev_b32_e32 v28, 16, v155
	v_and_b32_e32 v29, 0xffff0000, v155
	v_rcp_f32_e32 v11, v2
	v_add_f32_e32 v2, 1.0, v4
	v_pk_fma_f32 v[24:25], v[30:31], v[28:29], v[24:25]
	v_lshlrev_b32_e32 v28, 16, v153
	v_and_b32_e32 v29, 0xffff0000, v153
	v_rcp_f32_e32 v4, v2
	v_add_f32_e32 v2, 1.0, v5
	v_pk_fma_f32 v[24:25], v[26:27], v[28:29], v[24:25]
	v_lshlrev_b32_e32 v26, 16, v151
	v_and_b32_e32 v27, 0xffff0000, v151
	v_rcp_f32_e32 v5, v2
	v_mul_f32_e64 v2, v225, -v6
	v_pk_fma_f32 v[22:23], v[22:23], v[26:27], v[24:25]
	s_mov_b32 s4, 0x50000
	v_mul_f32_e32 v2, 0x3fb8aa3b, v2
	v_mul_f32_e64 v6, v225, -v7
	v_cvt_pk_bf16_f32 v20, v20, v21
	v_cvt_pk_bf16_f32 v21, v22, v23
	v_add_co_u32_e32 v22, vcc, s4, v116
	v_exp_f32_e32 v2, v2
	v_mul_f32_e32 v6, 0x3fb8aa3b, v6
	v_addc_co_u32_e32 v23, vcc, 0, v117, vcc
	v_exp_f32_e32 v7, v6
	global_store_dwordx2 v[22:23], v[20:21], off
	s_waitcnt vmcnt(10)
	v_lshlrev_b32_e32 v20, 16, v146
	v_and_b32_e32 v21, 0xffff0000, v146
	v_pk_fma_f32 v[16:17], v[16:17], v[20:21], 0 op_sel_hi:[1,1,0]
	s_waitcnt vmcnt(9)
	v_lshlrev_b32_e32 v20, 16, v144
	v_and_b32_e32 v21, 0xffff0000, v144
	v_pk_fma_f32 v[12:13], v[12:13], v[20:21], v[16:17]
	s_waitcnt vmcnt(8)
	v_lshlrev_b32_e32 v16, 16, v142
	v_and_b32_e32 v17, 0xffff0000, v142
	v_add_f32_e32 v2, 1.0, v2
	v_pk_fma_f32 v[8:9], v[8:9], v[16:17], v[12:13]
	s_waitcnt vmcnt(7)
	v_lshlrev_b32_e32 v12, 16, v140
	v_and_b32_e32 v13, 0xffff0000, v140
	v_rcp_f32_e32 v6, v2
	v_add_f32_e32 v2, 1.0, v7
	v_pk_fma_f32 v[4:5], v[4:5], v[12:13], v[8:9]
	v_lshlrev_b32_e32 v8, 16, v147
	v_and_b32_e32 v9, 0xffff0000, v147
	v_lshlrev_b32_e32 v12, 16, v145
	v_and_b32_e32 v13, 0xffff0000, v145
	v_rcp_f32_e32 v7, v2
	v_cvt_pk_bf16_f32 v4, v4, v5
	v_pk_fma_f32 v[8:9], v[18:19], v[8:9], 0 op_sel_hi:[1,1,0]
	v_pk_fma_f32 v[8:9], v[14:15], v[12:13], v[8:9]
	v_lshlrev_b32_e32 v12, 16, v143
	v_and_b32_e32 v13, 0xffff0000, v143
	v_pk_fma_f32 v[8:9], v[10:11], v[12:13], v[8:9]
	v_lshlrev_b32_e32 v10, 16, v141
	v_and_b32_e32 v11, 0xffff0000, v141
	v_pk_fma_f32 v[6:7], v[6:7], v[10:11], v[8:9]
	v_cvt_pk_bf16_f32 v5, v6, v7
	v_add_co_u32_e32 v6, vcc, 0x58000, v116
	s_mov_b64 s[4:5], -1
	s_nop 0
	v_addc_co_u32_e32 v7, vcc, 0, v117, vcc
	s_andn2_b64 vcc, exec, s[38:39]
	s_mov_b32 s77, 0xc000
	s_mov_b32 s76, 0xe000
	s_movk_i32 s75, 0x3400
	v_readlane_b32 s74, v255, 38
	global_store_dwordx2 v[6:7], v[4:5], off
	s_cbranch_vccnz .LBB0_1036
	s_andn2_b64 vcc, exec, s[10:11]
	s_cbranch_vccnz .LBB0_1035
	s_barrier
	s_branch .LBB0_1035
